# P5 and P6: workgroups on XCDs 4-7 start ~13us late so the two halves of the chip run their HBM-bound epilogues at different times
# baseline (speedup 1.0000x reference)
;     __device__ __forceinline__ const char* a_base(const Unit& u) const { return (const char*)A + (size_t)u.pm * BM * lda * 2; }
;     __device__ __forceinline__ const char* b_base(const Unit& u) const { return (const char*)Bt + (size_t)u.pn * BM * K * 2; }
;     __device__ __forceinline__ const char* b_base(const Unit& u) const { return (const char*)Bt + ((size_t)u.e * NB + (size_t)u.pn * BM) * K * 2; }
; #define PG8_RC() int R[2], C[2]; { int t_ = threadIdx.x; asm volatile("" : "+v"(t_)); _Pragma("unroll") for (int i = 0; i < 2; ++i) stage_rc(t_ * 16 + i * 8192, R[i], C[i]); }
; #define PG8_STAGEB(bufoff, gbase) PG8_STAGE2(bufoff, gbase, voffB[0], voffB[1])
; #define PG8_STAGEA(bufoff, gbase, h) PG8_STAGE2(bufoff, gbase, voffA[h][0], voffA[h][1])
; #define REP(k) for (int rep_ = reframe(F); rep_ < (((MK_DUP) >> (k)) & 1) + 1; ++rep_)
;     ...
;     Unit cur, nxt; int ui = 0;
;     if (!S.next(0, cur)) return;
;     unsigned voffA[2][2];
;     { PG8_RC(); S.a_offs(cur, R, C, voffA); }
;     f32x4 acc[2][2][4][2];
; #pragma unroll
;     for (int a = 0; a < 2; ++a)
; #pragma unroll
;         for (int b = 0; b < 2; ++b)
; #pragma unroll
;             for (int m = 0; m < 4; ++m)
; #pragma unroll
;                 for (int n = 0; n < 2; ++n) acc[a][b][m][n] = (f32x4){0.f, 0.f, 0.f, 0.f};
;     bf16x8 At[4][2], B0[2][2], B1[2][2];
;     const char* cA = S.a_base(cur); const char* cB = S.b_base(cur);
;     const unsigned bias_lds = (unsigned)__builtin_amdgcn_readfirstlane((int)((unsigned)(size_t)lds + (unsigned)(AUX_OFF + 8192) + (unsigned)wid * 256u));
;     if constexpr (Epi::kBiasDMA) { if (lane < 16) glds16(E.bias_base(cur), E.bias_off(cur, wc, lane), bias_lds); }
;     const unsigned rowid_lds = (unsigned)__builtin_amdgcn_readfirstlane((int)((unsigned)(size_t)lds + (unsigned)AUX_OFF + (unsigned)wid * 512u));
;     if constexpr (Epi::kRowDMA) { if (lane < 32) glds16(E.row_base(cur), E.row_off(cur, wr, lane), rowid_lds); }
;     PG8_STAGEB(PG8_SB(0, 0), cB); PG8_STAGEB(PG8_SB(0, 1), cB + hstepB); PG8_STAGEA(PG8_SA(0, 0), cA, 0); if constexpr (!HM) PG8_STAGEA(PG8_SA(0, 1), cA, 1);
; __global__ void __launch_bounds__(NTHREADS, 2) mk_fwd(Args args) {
;     ...
;     if (IN(5)) REP(5) {
;         { pg8::DenseSched S; S.init((const bf16_t*)(F.ws + WS_SG), GW, (const bf16_t*)(F.ws + WS_WPA), GW, T, D, F.G, (int)blockIdx.x); EpiMerge<0> E{F.ws}; pg8::gemm_phase<0>(F.lds, S, E); }
.LBB0_559:
	s_cmp_lt_i32 s88, 6
	s_cselect_b64 s[4:5], -1, 0
	s_and_b64 s[4:5], s[4:5], s[0:1]
	s_andn2_b64 vcc, exec, s[4:5]
	s_cbranch_vccnz .LBB0_620
	s_and_b32 s98, s92, 4
	s_cmp_eq_u32 s98, 0
	s_cbranch_scc1 .Lstag5_done
	s_sleep 127
	s_sleep 127
	s_sleep 127
.Lstag5_done:
	s_cmpk_lt_i32 s92, 0x200
	s_cselect_b64 s[12:13], -1, 0
	s_waitcnt lgkmcnt(0)
	s_add_u32 s8, s94, 0x63000000
	s_addc_u32 s9, s95, 0
	s_ashr_i32 s33, s92, 31
	s_lshr_b32 s0, s33, 29
	v_mov_b32_e32 v1, v0
	s_add_i32 s0, s92, s0
	s_waitcnt vmcnt(2)
	v_mov_b32_e32 v2, 0x7f7f7f7f
	v_mov_b32_e32 v3, 0x7f7f7f7f
	s_ashr_i32 s48, s0, 3
	s_and_b32 s0, s0, -8
	s_ashr_i32 s3, s2, 31
	s_sub_i32 s50, s92, s0
	v_mov_b32_e32 v2, v0
	s_cmp_lt_i32 s50, 0
	s_cselect_b64 s[10:11], -1, 0
	v_readfirstlane_b32 s1, v2
	s_lshl_b32 s49, s50, 6
	s_ashr_i32 s6, s1, 6
	v_mov_b32_e32 v1, 0x7f7f7f7f
	s_cmpk_gt_i32 s92, 0x1ff
	s_mulk_i32 s50, 0x41
	s_cbranch_scc1 .LBB0_590
	v_bfe_i32 v5, v2, 27, 1
	v_lshlrev_b32_e32 v3, 4, v2
	v_lshrrev_b32_e32 v5, 22, v5
	v_add_u32_e32 v5, v3, v5
	v_and_b32_e32 v5, 0xfffffc00, v5
	v_sub_u32_e32 v5, v3, v5
	s_waitcnt vmcnt(1)
	v_lshrrev_b32_e32 v6, 4, v5
	v_ashrrev_i32_e32 v4, 31, v2
	v_bitop3_b32 v5, v6, v5, 32 bitop3:0x6c
	v_lshrrev_b32_e32 v4, 26, v4
	v_ashrrev_i32_e32 v7, 31, v5
	v_add_u32_e32 v4, v2, v4
	v_lshrrev_b32_e32 v7, 26, v7
	v_ashrrev_i32_e32 v4, 6, v4
	v_add_u32_e32 v7, v5, v7
	v_lshlrev_b32_e32 v6, 3, v4
	v_lshrrev_b32_e32 v8, 6, v7
	v_and_b32_e32 v7, 0xc0, v7
	v_and_b32_e32 v6, 0x1ffff0, v6
	v_lshlrev_b32_e32 v4, 5, v4
	v_sub_u32_e32 v5, v5, v7
	v_mov_b32_e32 v7, 1
	v_add_u32_e32 v6, v8, v6
	v_and_b32_e32 v4, 32, v4
	v_ashrrev_i16_sdwa v5, v7, sext(v5) dst_sel:DWORD dst_unused:UNUSED_PAD src0_sel:DWORD src1_sel:BYTE_0
	v_bfe_i32 v5, v5, 0, 16
	v_lshl_or_b32 v4, v6, 10, v4
	v_add_u32_e32 v3, 0x2000, v3
	v_add_lshl_u32 v158, v4, v5, 1
	v_ashrrev_i32_e32 v4, 31, v3
	v_lshrrev_b32_e32 v4, 22, v4
	v_add_u32_e32 v4, v3, v4
	v_ashrrev_i32_e32 v4, 10, v4
	v_mul_i32_i24_e32 v5, 0x400, v4
	v_sub_u32_e32 v3, v3, v5
	v_lshrrev_b32_e32 v5, 4, v3
	v_bitop3_b32 v3, v5, v3, 32 bitop3:0x6c
	v_ashrrev_i32_e32 v6, 31, v3
	v_lshrrev_b32_e32 v6, 26, v6
	v_add_u32_e32 v6, v3, v6
	v_lshlrev_b32_e32 v5, 3, v4
	v_lshrrev_b32_e32 v8, 6, v6
	v_and_b32_e32 v6, 0xc0, v6
	v_and_b32_e32 v5, 0x1ffff0, v5
	v_lshlrev_b32_e32 v4, 5, v4
	v_sub_u32_e32 v3, v3, v6
	v_add_u32_e32 v5, v8, v5
	v_and_b32_e32 v4, 32, v4
	v_ashrrev_i16_sdwa v3, v7, sext(v3) dst_sel:DWORD dst_unused:UNUSED_PAD src0_sel:DWORD src1_sel:BYTE_0
	v_bfe_i32 v3, v3, 0, 16
	v_lshl_or_b32 v4, v5, 10, v4
	s_add_u32 s51, s94, 0x51000000
	v_add_lshl_u32 v159, v4, v3, 1
	v_mov_b32_e32 v3, v0
	s_addc_u32 s52, s95, 0
	s_add_u32 s53, s94, 0x3200000
	v_ashrrev_i32_e32 v5, 31, v3
	v_lshrrev_b32_e32 v5, 26, v5
	s_addc_u32 s54, s95, 0
	s_lshl_b32 s0, s6, 10
	v_lshlrev_b32_e32 v4, 4, v3
	v_add_u32_e32 v5, v3, v5
	v_bfe_i32 v3, v3, 27, 1
	s_ashr_i32 s7, s1, 8
	s_add_i32 s55, s0, 0
	v_lshrrev_b32_e32 v3, 22, v3
	s_and_b64 s[14:15], s[10:11], exec
	v_add_u32_e32 v3, v4, v3
	s_cselect_b32 s0, s50, s49
	v_and_b32_e32 v3, 0xfffffc00, v3
	s_add_i32 s0, s0, s48
	v_sub_u32_e32 v3, v4, v3
	s_ashr_i32 s14, s0, 31
	v_lshrrev_b32_e32 v6, 4, v3
	s_lshr_b32 s14, s14, 27
	v_bitop3_b32 v3, v6, v3, 32 bitop3:0x6c
	s_add_i32 s14, s0, s14
	v_ashrrev_i32_e32 v8, 31, v3
	s_ashr_i32 s15, s14, 5
	s_andn2_b32 s14, s14, 31
	v_lshrrev_b32_e32 v8, 26, v8
	s_sub_i32 s14, s0, s14
	v_add_u32_e32 v8, v3, v8
	s_bfe_i32 s0, s14, 0x80000
	v_ashrrev_i32_e32 v5, 6, v5
	v_ashrrev_i32_e32 v9, 6, v8
	v_and_b32_e32 v8, 0xc0, v8
	s_bfe_u32 s0, s0, 0x2000d
	v_lshlrev_b32_e32 v6, 3, v5
	v_lshlrev_b32_e32 v5, 5, v5
	v_sub_u32_e32 v3, v3, v8
	s_add_i32 s16, s14, s0
	v_and_b32_e32 v5, 32, v5
	v_ashrrev_i16_sdwa v3, v7, sext(v3) dst_sel:DWORD dst_unused:UNUSED_PAD src0_sel:DWORD src1_sel:BYTE_0
	v_add_u32_e32 v4, 0x2000, v4
	s_bfe_i32 s0, s16, 0x80000
	s_and_b32 s16, s16, 0xfc
	v_add_u32_sdwa v3, v5, sext(v3) dst_sel:DWORD dst_unused:UNUSED_PAD src0_sel:DWORD src1_sel:WORD_0
	v_ashrrev_i32_e32 v5, 31, v4
	s_sub_i32 s14, s14, s16
	v_lshrrev_b32_e32 v5, 22, v5
	s_lshl_b32 s15, s15, 2
	s_sext_i32_i8 s14, s14
	v_add_u32_e32 v5, v4, v5
	s_add_i32 s36, s15, s14
	v_ashrrev_i32_e32 v5, 10, v5
	s_sext_i32_i16 s0, s0
	v_mul_i32_i24_e32 v8, 0x400, v5
	s_ashr_i32 s37, s36, 31
	s_lshr_b32 s0, s0, 2
	v_sub_u32_e32 v4, v4, v8
	s_lshl_b64 s[14:15], s[36:37], 19
	v_lshrrev_b32_e32 v8, 4, v4
	s_add_u32 s38, s51, s14
	v_and_b32_e32 v6, -16, v6
	v_bitop3_b32 v4, v8, v4, 32 bitop3:0x6c
	s_addc_u32 s39, s52, s15
	s_bfe_i64 s[14:15], s[0:1], 0x100000
	v_add_u32_e32 v6, v9, v6
	v_ashrrev_i32_e32 v9, 31, v4
	s_lshl_b64 s[14:15], s[14:15], 19
	v_lshrrev_b32_e32 v9, 26, v9
	s_add_u32 s40, s53, s14
	v_add_u32_e32 v9, v4, v9
	s_addc_u32 s41, s54, s15
	s_add_i32 s37, s55, 0x10000
	s_mov_b32 s14, m0
	s_mov_b32 m0, s37
	s_nop 0
	global_load_lds_dwordx4 v158, s[40:41]
	s_mov_b32 m0, s14
	v_ashrrev_i32_e32 v10, 6, v9
	v_and_b32_e32 v9, 0xc0, v9
	s_add_i32 s56, s55, 0x12000
	s_mov_b32 s14, m0
	s_mov_b32 m0, s56
	s_nop 0
	global_load_lds_dwordx4 v159, s[40:41]
	s_mov_b32 m0, s14
	v_lshlrev_b32_e32 v8, 3, v5
	v_lshlrev_b32_e32 v5, 5, v5
	v_sub_u32_e32 v4, v4, v9
	s_add_u32 s14, s40, 0x40000
	v_and_b32_e32 v8, -16, v8
	v_and_b32_e32 v5, 32, v5
	v_ashrrev_i16_sdwa v4, v7, sext(v4) dst_sel:DWORD dst_unused:UNUSED_PAD src0_sel:DWORD src1_sel:BYTE_0
	s_addc_u32 s15, s41, 0
	s_add_i32 s57, s55, 0x14000
	s_mov_b32 s16, m0
	s_mov_b32 m0, s57
	s_nop 0
	global_load_lds_dwordx4 v158, s[14:15]
	s_mov_b32 m0, s16
	v_add_u32_e32 v8, v10, v8
	v_add_u32_sdwa v4, v5, sext(v4) dst_sel:DWORD dst_unused:UNUSED_PAD src0_sel:DWORD src1_sel:WORD_0
	v_lshl_add_u32 v5, v6, 10, v3
	v_lshlrev_b32_e32 v6, 11, v6
	s_add_i32 s58, s55, 0x16000
	s_mov_b32 s16, m0
	s_mov_b32 m0, s58
	s_nop 0
	global_load_lds_dwordx4 v159, s[14:15]
	s_mov_b32 m0, s16
	v_lshl_add_u32 v160, v3, 1, v6
	v_lshlrev_b32_e32 v3, 11, v8
	s_mov_b32 s14, m0
	s_mov_b32 m0, s55
	s_nop 0
	global_load_lds_dwordx4 v160, s[38:39]
	s_mov_b32 m0, s14
	v_lshl_add_u32 v161, v4, 1, v3
	v_mov_b32_e32 v3, 0x40000
	s_add_i32 s59, s55, 0x2000
	s_mov_b32 s14, m0
	s_mov_b32 m0, s59
	s_nop 0
	global_load_lds_dwordx4 v161, s[38:39]
	s_mov_b32 m0, s14
	v_lshl_add_u32 v7, v8, 10, v4
	v_lshl_add_u32 v162, v5, 1, v3
	s_add_i32 s60, s55, 0x4000
	s_mov_b32 s14, m0
	s_mov_b32 m0, s60
	s_nop 0
	global_load_lds_dwordx4 v162, s[38:39]
	s_mov_b32 m0, s14
	v_lshl_add_u32 v163, v7, 1, v3
	s_add_i32 s61, s55, 0x6000
	s_mov_b32 s16, m0
	s_mov_b32 m0, s61
	s_nop 0
	global_load_lds_dwordx4 v163, s[38:39]
	s_mov_b32 m0, s16
	s_cmp_eq_u32 s7, 1
	s_cselect_b64 s[14:15], -1, 0
	s_cmp_lg_u32 s7, 1
	s_cbranch_scc1 .LBB0_563
	s_barrier

; #define REP(k) for (int rep_ = reframe(F); rep_ < (((MK_DUP) >> (k)) & 1) + 1; ++rep_)
;     __device__ __forceinline__ bool next(int i, Unit& u) const {
;         const long L = (long)i * G + c; if (L >= nwg) return false;
;         int wgid = (int)L; { const int q = nwg / NXCD, r = nwg % NXCD, xcd = wgid % NXCD, off = wgid / NXCD; wgid = (xcd < r ? xcd * (q + 1) : r * (q + 1) + (xcd - r) * q) + off; }
;         const int nig = WGM * nN, gid = wgid / nig, fm = gid * WGM, gsz = (nM - fm) < WGM ? (nM - fm) : WGM;
;         u.pm = fm + ((wgid % nig) % gsz); u.pn = (wgid % nig) / gsz; u.e = 0; u.mt = u.pm; u.hx = 0; return true;
; __global__ void __launch_bounds__(NTHREADS, 2) mk_fwd(Args args) {
;     ...
;     if (IN(6)) REP(6) {
;         pg8::DenseSched S; S.init((const bf16_t*)(F.ws + WS_MRG), D, (const bf16_t*)(F.ws + WS_WOUT), D, T, D, F.G, (int)blockIdx.x);
.LBB0_674:
	s_cmp_lt_i32 s88, 7
	s_cselect_b64 s[4:5], -1, 0
	s_and_b64 s[4:5], s[4:5], s[0:1]
	s_andn2_b64 vcc, exec, s[4:5]
	s_cbranch_vccnz .LBB0_723
	s_and_b32 s98, s92, 4
	s_cmp_eq_u32 s98, 0
	s_cbranch_scc1 .Lstag6_done
	s_sleep 127
	s_sleep 127
	s_sleep 127
.Lstag6_done:
	v_mov_b32_e32 v1, v0
	s_waitcnt vmcnt(2)
	v_mov_b32_e32 v2, 0x7f7f7f7f
	v_mov_b32_e32 v1, 0x7f7f7f7f
	s_cmpk_lt_i32 s92, 0x200
	v_mov_b32_e32 v2, v0
	s_cselect_b64 s[0:1], -1, 0
	v_readfirstlane_b32 s6, v2
	s_ashr_i32 s7, s6, 6
	s_cmpk_gt_i32 s92, 0x1ff
	s_cbranch_scc1 .LBB0_677
	s_ashr_i32 s3, s92, 31
	s_lshr_b32 s3, s3, 29
	s_add_i32 s3, s92, s3
	s_and_b32 s8, s3, -8
	s_sub_i32 s8, s92, s8
	s_lshl_b32 s10, s8, 6
	s_ashr_i32 s3, s3, 3
	s_mul_i32 s9, s8, 0x41
	s_cmp_lt_i32 s8, 0
	s_cselect_b32 s8, s9, s10
	s_add_i32 s3, s8, s3
	s_ashr_i32 s8, s3, 31
	s_lshr_b32 s8, s8, 27
	s_add_i32 s8, s3, s8
	s_ashr_i32 s9, s8, 5
	s_andn2_b32 s8, s8, 31
	s_sub_i32 s3, s3, s8
	s_bfe_i32 s8, s3, 0x80000
	s_bfe_u32 s8, s8, 0x2000d
	s_add_i32 s8, s3, s8
	s_bfe_i32 s10, s8, 0x80000
	s_and_b32 s8, s8, 0xfc
	s_sub_i32 s3, s3, s8
	s_lshl_b32 s9, s9, 2
	s_sext_i32_i16 s10, s10
	s_sext_i32_i8 s3, s3
	s_add_i32 s26, s9, s3
	s_ashr_i32 s24, s10, 2

; __global__ void __launch_bounds__(NTHREADS, 2) mk_fwd(Args args) {
	.amdhsa_kernel _Z6mk_fwd4Args
		.amdhsa_group_segment_fixed_size 0
		.amdhsa_private_segment_fixed_size 0
		.amdhsa_kernarg_size 456
		.amdhsa_user_sgpr_count 2
		.amdhsa_user_sgpr_dispatch_ptr 0
		.amdhsa_user_sgpr_queue_ptr 0
		.amdhsa_user_sgpr_kernarg_segment_ptr 1
		.amdhsa_user_sgpr_dispatch_id 0
		.amdhsa_user_sgpr_kernarg_preload_length 0
		.amdhsa_user_sgpr_kernarg_preload_offset 0
		.amdhsa_user_sgpr_private_segment_size 0
		.amdhsa_uses_dynamic_stack 0
		.amdhsa_enable_private_segment 0
		.amdhsa_system_sgpr_workgroup_id_x 1
		.amdhsa_system_sgpr_workgroup_id_y 0
		.amdhsa_system_sgpr_workgroup_id_z 0
		.amdhsa_system_sgpr_workgroup_info 0
		.amdhsa_system_vgpr_workitem_id 0
		.amdhsa_next_free_vgpr 255
		.amdhsa_next_free_sgpr 102
		.amdhsa_accum_offset 256
		.amdhsa_reserve_vcc 1
		.amdhsa_float_round_mode_32 0
		.amdhsa_float_round_mode_16_64 0
		.amdhsa_float_denorm_mode_32 3
		.amdhsa_float_denorm_mode_16_64 3
		.amdhsa_dx10_clamp 1
		.amdhsa_ieee_mode 1
		.amdhsa_fp16_overflow 0
		.amdhsa_tg_split 0
		.amdhsa_exception_fp_ieee_invalid_op 0
		.amdhsa_exception_fp_denorm_src 0
		.amdhsa_exception_fp_ieee_div_zero 0
		.amdhsa_exception_fp_ieee_overflow 0
		.amdhsa_exception_fp_ieee_underflow 0
		.amdhsa_exception_fp_ieee_inexact 0
		.amdhsa_exception_int_div_zero 0
	.end_amdhsa_kernel

; __global__ void __launch_bounds__(NTHREADS, 2) mk_fwd(Args args) {
amdhsa.kernels:
  - .agpr_count:     0
    .args:
      - .offset:         0
        .size:           200
        .value_kind:     by_value
      - .offset:         200
        .size:           4
        .value_kind:     hidden_block_count_x
      - .offset:         204
        .size:           4
        .value_kind:     hidden_block_count_y
      - .offset:         208
        .size:           4
        .value_kind:     hidden_block_count_z
      - .offset:         212
        .size:           2
        .value_kind:     hidden_group_size_x
      - .offset:         214
        .size:           2
        .value_kind:     hidden_group_size_y
      - .offset:         216
        .size:           2
        .value_kind:     hidden_group_size_z
      - .offset:         218
        .size:           2
        .value_kind:     hidden_remainder_x
      - .offset:         220
        .size:           2
        .value_kind:     hidden_remainder_y
      - .offset:         222
        .size:           2
        .value_kind:     hidden_remainder_z
      - .offset:         240
        .size:           8
        .value_kind:     hidden_global_offset_x
      - .offset:         248
        .size:           8
        .value_kind:     hidden_global_offset_y
      - .offset:         256
        .size:           8
        .value_kind:     hidden_global_offset_z
      - .offset:         264
        .size:           2
        .value_kind:     hidden_grid_dims
      - .offset:         320
        .size:           4
        .value_kind:     hidden_dynamic_lds_size
    .group_segment_fixed_size: 0
    .kernarg_segment_align: 8
    .kernarg_segment_size: 456
    .language:       OpenCL C
    .language_version:
      - 2
      - 0
    .max_flat_workgroup_size: 512
    .name:           _Z6mk_fwd4Args
    .private_segment_fixed_size: 0
    .sgpr_count:     108
    .sgpr_spill_count: 72
    .symbol:         _Z6mk_fwd4Args.kd
    .uniform_work_group_size: 1
    .uses_dynamic_stack: false
    .vgpr_count:     255
    .vgpr_spill_count: 0
    .wavefront_size: 64
